# speedup vs baseline: 1.0230x; 1.0230x over previous
_Z6k_gemmPKfS0_PK15HIP_vector_typeIjLj4EEPDF16_PKh:
	s_load_dwordx4 s[20:23], s[0:1], 0x0
	s_load_dwordx4 s[4:7], s[0:1], 0x10
	s_load_dwordx2 s[38:39], s[0:1], 0x20
	v_readfirstlane_b32 s8, v0
	v_and_b32_e32 v1, 63, v0
	s_nop 3
	s_lshr_b32 s8, s8, 6
	s_and_b32 s40, s2, 7
	s_lshr_b32 s41, s2, 3
	s_mul_i32 s18, s40, 0x187
	s_add_u32 s19, s18, 0x187
	s_min_u32 s19, s19, 0xc35
	s_sub_u32 s33, s19, s18
	s_sub_u32 s33, s33, 0x180
	s_lshl_b32 s33, s33, 2
	s_cmp_lt_u32 s41, s33
	s_cselect_b32 s44, 7, 6
	s_lshr_b32 s45, s41, 2
	s_add_u32 s45, s45, s18
	s_add_u32 s45, s45, 0x180
	s_lshl_b32 s45, s45, 4
	s_and_b32 s46, s41, 3
	s_lshl_b32 s46, s46, 2
	s_add_u32 s47, s45, s46
	s_mul_i32 s45, s47, 0x4b0
	s_lshl_b32 s46, s47, 8
	s_add_i32 s18, s18, s41
	s_cmp_eq_u32 s8, 0
	s_cselect_b32 s9, s44, 6
	s_add_i32 s11, s44, 4
	s_lshl_b32 s18, s18, 4
	s_lshl_b32 s19, s8, 2
	s_add_i32 s33, s18, s19
	s_mul_i32 s12, s33, 0x4b0
	s_lshl_b32 s32, s18, 8
	s_sub_u32 s32, s32, 0x100000
	s_mov_b32 s10, 0
	v_lshl_add_u32 v253, v1, 10, s33
	v_mov_b32_e32 v254, s47
	v_cmp_eq_u32_e32 vcc, 6, v1
	s_nop 1
	v_cndmask_b32_e32 v253, v253, v254, vcc
	v_mov_b32_e32 v247, 0
	v_cmp_gt_i32_e32 vcc, s9, v1
	s_mov_b32 s18, 0xc350
	v_cmp_gt_i32_e64 s[36:37], s18, v253
	s_and_b64 vcc, vcc, s[36:37]
	s_waitcnt lgkmcnt(0)
	s_and_saveexec_b64 s[36:37], vcc
	global_load_dword v247, v253, s[38:39]
	s_mov_b64 exec, s[36:37]
	s_mov_b32 s24, s22
	s_and_b32 s25, s23, 0xffff
	s_mov_b32 s26, 0x3938700
	s_mov_b32 s27, 0x20000
	s_and_b32 s21, s21, 0xffff
	s_mov_b32 s22, 0x3938700
	s_mov_b32 s23, 0x20000
	s_mov_b32 s28, s6
	s_and_b32 s29, s7, 0xffff
	s_mov_b32 s30, 0xc35000
	s_mov_b32 s31, 0x20000
	v_lshlrev_b32_e32 v238, 4, v1
	v_mul_u32_u24_e32 v253, 0x1746, v1
	v_lshrrev_b32_e32 v253, 16, v253
	v_min_u32_e32 v253, 3, v253
	v_mul_u32_u24_e32 v254, 11, v253
	v_sub_u32_e32 v254, v1, v254
	v_lshlrev_b32_e32 v240, 3, v253
	v_mul_u32_u24_e32 v249, 0x4b0, v253
	v_lshl_add_u32 v249, v254, 4, v249
	v_add_u32_e32 v249, 0x400, v249
	v_mov_b32_e32 v255, 0x80000000
	v_cmp_gt_u32_e64 s[34:35], 44, v1
	s_nop 1
	v_cndmask_b32_e64 v239, v255, v249, s[34:35]
	v_lshl_add_u32 v250, s8, 2, v253
	v_mul_u32_u24_e32 v250, 0x4e0, v250
	v_lshl_add_u32 v250, v254, 3, v250
	v_add_u32_e32 v242, 0x200, v250
	s_mul_i32 s18, s8, 0x1380
	v_lshl_add_u32 v241, v1, 3, s18
	v_and_b32_e32 v249, 15, v1
	v_lshrrev_b32_e32 v250, 4, v1
	v_mul_u32_u24_e32 v243, 0x4e0, v249
	v_lshl_add_u32 v243, v250, 4, v243
	v_mul_u32_u24_e32 v244, 0x440, v250
	v_lshl_add_u32 v244, v249, 1, v244
	s_lshl_b32 s18, s8, 6
	s_add_i32 s18, s18, 39936
	v_add_u32_e32 v244, s18, v244
	v_lshrrev_b32_e32 v249, 4, v0
	v_and_b32_e32 v250, 15, v0
	v_mul_u32_u24_e32 v245, 0x110, v249
	v_lshl_add_u32 v245, v250, 4, v245
	v_add_u32_e32 v245, 39936, v245
	v_lshlrev_b32_e32 v246, 8, v249
	v_lshl_add_u32 v246, v250, 4, v246
	s_lshl_b32 s18, s8, 12
	s_add_i32 s18, s18, 48640
	v_lshl_add_u32 v248, v1, 4, s18
	v_cmp_gt_u32_e32 vcc, 32, v0
	s_and_saveexec_b64 s[36:37], vcc
	v_mul_u32_u24_e32 v251, 0x4e00, v249
	v_mul_u32_u24_e32 v252, 0x4e0, v250
	v_add_u32_e32 v254, v251, v252
	v_mov_b32_e32 v250, 0
	v_mov_b32_e32 v251, 0
	v_mov_b32_e32 v252, 0
	v_mov_b32_e32 v253, 0
	ds_write_b128 v254, v[250:253] offset:1200
	s_mov_b64 exec, s[36:37]
	s_lshl_b32 s18, s8, 11
	v_lshl_add_u32 v253, v1, 4, s18
	v_add_u32_e32 v254, 0x22000, v253
	global_load_dwordx4 v[178:181], v254, s[4:5]
	global_load_dwordx4 v[182:185], v254, s[4:5] offset:1024
	v_add_u32_e32 v254, 0x2000, v254
	global_load_dwordx4 v[186:189], v254, s[4:5]
	global_load_dwordx4 v[190:193], v254, s[4:5] offset:1024
	v_mov_b32_e32 v236, v253
	s_waitcnt vmcnt(4)
	v_readlane_b32 s13, v247, s10
	s_add_u32 s14, s12, 0x4b0
	s_add_u32 s15, s12, 0x960
	s_add_u32 s16, s12, 0xe10
	s_nop 1
	s_and_b32 s18, s13, 0xff
	s_cmp_eq_u32 s18, 1
	s_cselect_b32 s42, s12, 0x80000000
	s_and_b32 s18, s13, 0xff00
	s_cmp_eq_u32 s18, 0x100
	s_cselect_b32 s14, s14, 0x80000000
	s_and_b32 s18, s13, 0xff0000
	s_cmp_eq_u32 s18, 0x10000
	s_cselect_b32 s15, s15, 0x80000000
	s_and_b32 s18, s13, 0xff000000
	s_cmp_eq_u32 s18, 0x1000000
	s_cselect_b32 s16, s16, 0x80000000
	v_lshrrev_b32_e64 v249, v240, s13
	v_and_b32_e32 v249, 0xff, v249
	v_cmp_eq_u32_e32 vcc, 1, v249
	s_nop 1
	v_cndmask_b32_e32 v254, v255, v239, vcc
	buffer_load_dwordx4 v[138:141], v238, s[20:23], s42 offen nt
	buffer_load_dwordx4 v[142:145], v238, s[24:27], s42 offen nt
	buffer_load_dwordx4 v[146:149], v238, s[20:23], s14 offen nt
	buffer_load_dwordx4 v[150:153], v238, s[24:27], s14 offen nt
	buffer_load_dwordx4 v[154:157], v238, s[20:23], s15 offen nt
	buffer_load_dwordx4 v[158:161], v238, s[24:27], s15 offen nt
	buffer_load_dwordx4 v[162:165], v238, s[20:23], s16 offen nt
	buffer_load_dwordx4 v[166:169], v238, s[24:27], s16 offen nt
	buffer_load_dwordx4 v[170:173], v254, s[20:23], s12 offen nt
	buffer_load_dwordx4 v[174:177], v254, s[24:27], s12 offen nt
	s_add_u32 s12, s12, 0x12c000
	s_add_u32 s32, s32, 0x40000
	s_mov_b32 s19, 0x80000000
	buffer_store_dwordx4 v[226:229], v246, s[28:31], s19 offen sc0 sc1
	s_mov_b32 s10, 1
	global_load_dwordx4 v[2:5], v236, s[4:5]
	global_load_dwordx4 v[6:9], v236, s[4:5] offset:1024
	v_add_u32_e32 v236, 0x2000, v236
	global_load_dwordx4 v[10:13], v236, s[4:5]
	global_load_dwordx4 v[14:17], v236, s[4:5] offset:1024
	v_add_u32_e32 v236, 0x2000, v236
	global_load_dwordx4 v[18:21], v236, s[4:5]
	global_load_dwordx4 v[22:25], v236, s[4:5] offset:1024
	v_add_u32_e32 v236, 0x2000, v236
	global_load_dwordx4 v[26:29], v236, s[4:5]
	global_load_dwordx4 v[30:33], v236, s[4:5] offset:1024
	v_add_u32_e32 v236, 0x2000, v236
	global_load_dwordx4 v[34:37], v236, s[4:5]
	global_load_dwordx4 v[38:41], v236, s[4:5] offset:1024
	v_add_u32_e32 v236, 0x2000, v236
	global_load_dwordx4 v[42:45], v236, s[4:5]
	global_load_dwordx4 v[46:49], v236, s[4:5] offset:1024
	v_add_u32_e32 v236, 0x2000, v236
	global_load_dwordx4 v[50:53], v236, s[4:5]
	global_load_dwordx4 v[54:57], v236, s[4:5] offset:1024
	v_add_u32_e32 v236, 0x2000, v236
	global_load_dwordx4 v[58:61], v236, s[4:5]
	global_load_dwordx4 v[62:65], v236, s[4:5] offset:1024
	v_add_u32_e32 v236, 0x2000, v236
	global_load_dwordx4 v[66:69], v236, s[4:5]
	global_load_dwordx4 v[70:73], v236, s[4:5] offset:1024
	v_add_u32_e32 v236, 0x2000, v236
	global_load_dwordx4 v[74:77], v236, s[4:5]
	global_load_dwordx4 v[78:81], v236, s[4:5] offset:1024
	v_add_u32_e32 v236, 0x2000, v236
	global_load_dwordx4 v[82:85], v236, s[4:5]
	global_load_dwordx4 v[86:89], v236, s[4:5] offset:1024
	v_add_u32_e32 v236, 0x2000, v236
	global_load_dwordx4 v[90:93], v236, s[4:5]
	global_load_dwordx4 v[94:97], v236, s[4:5] offset:1024
	v_add_u32_e32 v236, 0x2000, v236
	global_load_dwordx4 v[98:101], v236, s[4:5]
	global_load_dwordx4 v[102:105], v236, s[4:5] offset:1024
	v_add_u32_e32 v236, 0x2000, v236
	global_load_dwordx4 v[106:109], v236, s[4:5]
	global_load_dwordx4 v[110:113], v236, s[4:5] offset:1024
	v_add_u32_e32 v236, 0x2000, v236
	global_load_dwordx4 v[114:117], v236, s[4:5]
	global_load_dwordx4 v[118:121], v236, s[4:5] offset:1024
	v_add_u32_e32 v236, 0x2000, v236
	global_load_dwordx4 v[122:125], v236, s[4:5]
	global_load_dwordx4 v[126:129], v236, s[4:5] offset:1024
	v_add_u32_e32 v236, 0x2000, v236
	global_load_dwordx4 v[130:133], v236, s[4:5]
	global_load_dwordx4 v[134:137], v236, s[4:5] offset:1024
	s_waitcnt vmcnt(45)
	ds_write_b128 v248, v[178:181]
	ds_write_b128 v248, v[182:185] offset:1024
	ds_write_b128 v248, v[186:189] offset:2048
	ds_write_b128 v248, v[190:193] offset:3072
	s_waitcnt lgkmcnt(0)
	s_barrier
	s_branch .Lg_half1

.Lg_s3skip0:
	s_cmp_eq_u32 s10, 10
	s_cselect_b32 s32, s46, s32
	s_sub_u32 s18, s10, 4
	s_cmp_lt_u32 s18, s9
	s_cselect_b32 s19, s32, 0x80000000
	ds_read_b128 v[226:229], v245 offset:0
	s_add_u32 s32, s32, 0x40000
	s_waitcnt lgkmcnt(0)
	buffer_store_dwordx4 v[226:229], v246, s[28:31], s19 offen sc0 sc1
	s_barrier
	s_add_u32 s10, s10, 1
	s_cmp_ge_u32 s10, s11
	s_cbranch_scc1 .Lg_end

.Lg_s3skip1:
	s_cmp_eq_u32 s10, 10
	s_cselect_b32 s32, s46, s32
	s_sub_u32 s18, s10, 4
	s_cmp_lt_u32 s18, s9
	s_cselect_b32 s19, s32, 0x80000000
	ds_read_b128 v[226:229], v245 offset:4352
	s_add_u32 s32, s32, 0x40000
	s_waitcnt lgkmcnt(0)
	buffer_store_dwordx4 v[226:229], v246, s[28:31], s19 offen sc0 sc1
	s_barrier
	s_add_u32 s10, s10, 1
	s_cmp_lt_u32 s10, s11
	s_cbranch_scc1 .Lg_top
